# NSA top-k threshold search processes 4 tokens per trip with interleaved bit-serial chains (on top of hoisted GEMM constants, unscaled fp8 MFMA, NSA mask)
# baseline (speedup 1.0000x reference)
.LBB0_1692:
	s_add_i32 s3, s3, -4
	s_add_i32 s6, s6, 32
	s_cmp_eq_u32 s3, 0
	v_add_u32_e32 v4, 0x1040, v4
	s_cbranch_scc1 .LBB0_1705
.LBB0_1693:
	v_mov_b32_e32 v1, 0
	v_add_u32_e32 v0, 0x0, v4
	v_mov_b32_e32 v2, 0
	s_and_saveexec_b64 s[4:5], s[12:13]
	s_cbranch_execz .Ltk_a0
	v_add_u32_e32 v2, 0x10000, v0
	ds_read_b32 v2, v2
	s_waitcnt lgkmcnt(0)
	v_add_f32_e32 v2, 0, v2
.Ltk_a0:
	s_or_b64 exec, exec, s[4:5]
	s_and_saveexec_b64 s[4:5], s[14:15]
	s_cbranch_execz .Ltk_b0
	v_add_u32_e32 v1, 0x10004, v0
	ds_read_b32 v1, v1
.Ltk_b0:
	s_or_b64 exec, exec, s[4:5]
	v_mov_b32_e32 v5, 0
	s_and_saveexec_b64 s[4:5], s[16:17]
	s_cbranch_execz .Ltk_c0
	v_add_u32_e32 v5, 0x10008, v0
	ds_read_b32 v5, v5

.Ltk_e0:
	s_or_b64 exec, exec, s[4:5]
	v_cndmask_b32_e64 v0, v1, v171, s[10:11]
	v_cndmask_b32_e32 v220, v0, v169, vcc
	v_not_b32_e32 v0, v220
	v_or_b32_e32 v1, 0x80000000, v220
	v_cmp_gt_i32_e64 s[18:19], 0, v220
	s_nop 1
	v_cndmask_b32_e64 v2, v1, v0, s[18:19]
	v_lshlrev_b64 v[212:213], 6, v[2:3]
	v_or_b32_e32 v212, v212, v146
	v_mov_b32_e32 v1, 0
	v_add_u32_e32 v0, 0x410, v4
	v_mov_b32_e32 v2, 0
	s_and_saveexec_b64 s[4:5], s[12:13]
	s_cbranch_execz .Ltk_a1
	v_add_u32_e32 v2, 0x10000, v0
	ds_read_b32 v2, v2
	s_waitcnt lgkmcnt(0)
	v_add_f32_e32 v2, 0, v2

.Ltk_e1:
	s_or_b64 exec, exec, s[4:5]
	v_cndmask_b32_e64 v0, v1, v171, s[10:11]
	v_cndmask_b32_e32 v221, v0, v169, vcc
	v_not_b32_e32 v0, v221
	v_or_b32_e32 v1, 0x80000000, v221
	v_cmp_gt_i32_e64 s[18:19], 0, v221
	s_nop 1
	v_cndmask_b32_e64 v2, v1, v0, s[18:19]
	v_lshlrev_b64 v[214:215], 6, v[2:3]
	v_or_b32_e32 v214, v214, v146
	v_mov_b32_e32 v1, 0
	v_add_u32_e32 v0, 0x820, v4
	v_mov_b32_e32 v2, 0
	s_and_saveexec_b64 s[4:5], s[12:13]
	s_cbranch_execz .Ltk_a2
	v_add_u32_e32 v2, 0x10000, v0
	ds_read_b32 v2, v2
	s_waitcnt lgkmcnt(0)
	v_add_f32_e32 v2, 0, v2

.Ltk_e2:
	s_or_b64 exec, exec, s[4:5]
	v_cndmask_b32_e64 v0, v1, v171, s[10:11]
	v_cndmask_b32_e32 v222, v0, v169, vcc
	v_not_b32_e32 v0, v222
	v_or_b32_e32 v1, 0x80000000, v222
	v_cmp_gt_i32_e64 s[18:19], 0, v222
	s_nop 1
	v_cndmask_b32_e64 v2, v1, v0, s[18:19]
	v_lshlrev_b64 v[216:217], 6, v[2:3]
	v_or_b32_e32 v216, v216, v146
	v_mov_b32_e32 v1, 0
	v_add_u32_e32 v0, 0xc30, v4
	v_mov_b32_e32 v2, 0
	s_and_saveexec_b64 s[4:5], s[12:13]
	s_cbranch_execz .Ltk_a3
	v_add_u32_e32 v2, 0x10000, v0
	ds_read_b32 v2, v2
	s_waitcnt lgkmcnt(0)
	v_add_f32_e32 v2, 0, v2

.Ltk_e3:
	s_or_b64 exec, exec, s[4:5]
	v_cndmask_b32_e64 v0, v1, v171, s[10:11]
	v_cndmask_b32_e32 v223, v0, v169, vcc
	v_not_b32_e32 v0, v223
	v_or_b32_e32 v1, 0x80000000, v223
	v_cmp_gt_i32_e64 s[18:19], 0, v223
	s_nop 1
	v_cndmask_b32_e64 v2, v1, v0, s[18:19]
	v_lshlrev_b64 v[218:219], 6, v[2:3]
	v_or_b32_e32 v218, v218, v146
	s_mov_b32 s52, 0
	s_mov_b32 s32, 0
	s_mov_b32 s72, 0
	s_mov_b32 s37, 0
	s_mov_b32 s76, 0
	s_mov_b32 s75, 0
	s_mov_b32 s80, 0
	s_mov_b32 s79, 0
	s_or_b32 s53, s32, 0x20
	v_cmp_le_u64_e64 s[84:85], s[52:53], v[212:213]
	s_or_b32 s73, s37, 0x20
	v_cmp_le_u64_e64 s[86:87], s[72:73], v[214:215]
	s_or_b32 s77, s75, 0x20
	v_cmp_le_u64_e64 s[98:99], s[76:77], v[216:217]
	s_or_b32 s81, s79, 0x20
	v_cmp_le_u64_e64 s[100:101], s[80:81], v[218:219]
	s_bcnt1_i32_b64 s1, s[84:85]
	s_cmp_gt_i32 s1, 15
	s_cselect_b32 s32, s53, s32
	s_bcnt1_i32_b64 s1, s[86:87]
	s_cmp_gt_i32 s1, 15
	s_cselect_b32 s37, s73, s37
	s_bcnt1_i32_b64 s1, s[98:99]
	s_cmp_gt_i32 s1, 15
	s_cselect_b32 s75, s77, s75
	s_bcnt1_i32_b64 s1, s[100:101]
	s_cmp_gt_i32 s1, 15
	s_cselect_b32 s79, s81, s79
	s_or_b32 s53, s32, 0x10
	v_cmp_le_u64_e64 s[84:85], s[52:53], v[212:213]
	s_or_b32 s73, s37, 0x10
	v_cmp_le_u64_e64 s[86:87], s[72:73], v[214:215]
	s_or_b32 s77, s75, 0x10
	v_cmp_le_u64_e64 s[98:99], s[76:77], v[216:217]
	s_or_b32 s81, s79, 0x10
	v_cmp_le_u64_e64 s[100:101], s[80:81], v[218:219]
	s_bcnt1_i32_b64 s1, s[84:85]
	s_cmp_gt_i32 s1, 15
	s_cselect_b32 s32, s53, s32
	s_bcnt1_i32_b64 s1, s[86:87]
	s_cmp_gt_i32 s1, 15
	s_cselect_b32 s37, s73, s37
	s_bcnt1_i32_b64 s1, s[98:99]
	s_cmp_gt_i32 s1, 15
	s_cselect_b32 s75, s77, s75
	s_bcnt1_i32_b64 s1, s[100:101]
	s_cmp_gt_i32 s1, 15
	s_cselect_b32 s79, s81, s79
	s_or_b32 s53, s32, 0x8
	v_cmp_le_u64_e64 s[84:85], s[52:53], v[212:213]
	s_or_b32 s73, s37, 0x8
	v_cmp_le_u64_e64 s[86:87], s[72:73], v[214:215]
	s_or_b32 s77, s75, 0x8
	v_cmp_le_u64_e64 s[98:99], s[76:77], v[216:217]
	s_or_b32 s81, s79, 0x8
	v_cmp_le_u64_e64 s[100:101], s[80:81], v[218:219]
	s_bcnt1_i32_b64 s1, s[84:85]
	s_cmp_gt_i32 s1, 15
	s_cselect_b32 s32, s53, s32
	s_bcnt1_i32_b64 s1, s[86:87]
	s_cmp_gt_i32 s1, 15
	s_cselect_b32 s37, s73, s37
	s_bcnt1_i32_b64 s1, s[98:99]
	s_cmp_gt_i32 s1, 15
	s_cselect_b32 s75, s77, s75
	s_bcnt1_i32_b64 s1, s[100:101]
	s_cmp_gt_i32 s1, 15
	s_cselect_b32 s79, s81, s79
	s_or_b32 s53, s32, 0x4
	v_cmp_le_u64_e64 s[84:85], s[52:53], v[212:213]
	s_or_b32 s73, s37, 0x4
	v_cmp_le_u64_e64 s[86:87], s[72:73], v[214:215]
	s_or_b32 s77, s75, 0x4
	v_cmp_le_u64_e64 s[98:99], s[76:77], v[216:217]
	s_or_b32 s81, s79, 0x4
	v_cmp_le_u64_e64 s[100:101], s[80:81], v[218:219]
	s_bcnt1_i32_b64 s1, s[84:85]
	s_cmp_gt_i32 s1, 15
	s_cselect_b32 s32, s53, s32
	s_bcnt1_i32_b64 s1, s[86:87]
	s_cmp_gt_i32 s1, 15
	s_cselect_b32 s37, s73, s37
	s_bcnt1_i32_b64 s1, s[98:99]
	s_cmp_gt_i32 s1, 15
	s_cselect_b32 s75, s77, s75
	s_bcnt1_i32_b64 s1, s[100:101]
	s_cmp_gt_i32 s1, 15
	s_cselect_b32 s79, s81, s79
	s_or_b32 s53, s32, 0x2
	v_cmp_le_u64_e64 s[84:85], s[52:53], v[212:213]
	s_or_b32 s73, s37, 0x2
	v_cmp_le_u64_e64 s[86:87], s[72:73], v[214:215]
	s_or_b32 s77, s75, 0x2
	v_cmp_le_u64_e64 s[98:99], s[76:77], v[216:217]
	s_or_b32 s81, s79, 0x2
	v_cmp_le_u64_e64 s[100:101], s[80:81], v[218:219]
	s_bcnt1_i32_b64 s1, s[84:85]
	s_cmp_gt_i32 s1, 15
	s_cselect_b32 s32, s53, s32
	s_bcnt1_i32_b64 s1, s[86:87]
	s_cmp_gt_i32 s1, 15
	s_cselect_b32 s37, s73, s37
	s_bcnt1_i32_b64 s1, s[98:99]
	s_cmp_gt_i32 s1, 15
	s_cselect_b32 s75, s77, s75
	s_bcnt1_i32_b64 s1, s[100:101]
	s_cmp_gt_i32 s1, 15
	s_cselect_b32 s79, s81, s79
	s_or_b32 s53, s32, 0x1
	v_cmp_le_u64_e64 s[84:85], s[52:53], v[212:213]
	s_or_b32 s73, s37, 0x1
	v_cmp_le_u64_e64 s[86:87], s[72:73], v[214:215]
	s_or_b32 s77, s75, 0x1
	v_cmp_le_u64_e64 s[98:99], s[76:77], v[216:217]
	s_or_b32 s81, s79, 0x1
	v_cmp_le_u64_e64 s[100:101], s[80:81], v[218:219]
	s_bcnt1_i32_b64 s1, s[84:85]
	s_cmp_gt_i32 s1, 15
	s_cselect_b32 s32, s53, s32
	s_bcnt1_i32_b64 s1, s[86:87]
	s_cmp_gt_i32 s1, 15
	s_cselect_b32 s37, s73, s37
	s_bcnt1_i32_b64 s1, s[98:99]
	s_cmp_gt_i32 s1, 15
	s_cselect_b32 s75, s77, s75
	s_bcnt1_i32_b64 s1, s[100:101]
	s_cmp_gt_i32 s1, 15
	s_cselect_b32 s79, s81, s79
	s_mov_b32 s53, s32
	s_mov_b32 s32, 0
	s_mov_b32 s73, s37
	s_mov_b32 s37, 0
	s_mov_b32 s77, s75
	s_mov_b32 s75, 0
	s_mov_b32 s81, s79
	s_mov_b32 s79, 0
	s_or_b32 s52, s32, 0x80000000
	v_cmp_le_u64_e64 s[84:85], s[52:53], v[212:213]
	s_or_b32 s72, s37, 0x80000000
	v_cmp_le_u64_e64 s[86:87], s[72:73], v[214:215]
	s_or_b32 s76, s75, 0x80000000
	v_cmp_le_u64_e64 s[98:99], s[76:77], v[216:217]
	s_or_b32 s80, s79, 0x80000000
	v_cmp_le_u64_e64 s[100:101], s[80:81], v[218:219]
	s_bcnt1_i32_b64 s1, s[84:85]
	s_cmp_gt_i32 s1, 15
	s_cselect_b32 s32, s52, s32
	s_bcnt1_i32_b64 s1, s[86:87]
	s_cmp_gt_i32 s1, 15
	s_cselect_b32 s37, s72, s37
	s_bcnt1_i32_b64 s1, s[98:99]
	s_cmp_gt_i32 s1, 15
	s_cselect_b32 s75, s76, s75
	s_bcnt1_i32_b64 s1, s[100:101]
	s_cmp_gt_i32 s1, 15
	s_cselect_b32 s79, s80, s79
	s_or_b32 s52, s32, 0x40000000
	v_cmp_le_u64_e64 s[84:85], s[52:53], v[212:213]
	s_or_b32 s72, s37, 0x40000000
	v_cmp_le_u64_e64 s[86:87], s[72:73], v[214:215]
	s_or_b32 s76, s75, 0x40000000
	v_cmp_le_u64_e64 s[98:99], s[76:77], v[216:217]
	s_or_b32 s80, s79, 0x40000000
	v_cmp_le_u64_e64 s[100:101], s[80:81], v[218:219]
	s_bcnt1_i32_b64 s1, s[84:85]
	s_cmp_gt_i32 s1, 15
	s_cselect_b32 s32, s52, s32
	s_bcnt1_i32_b64 s1, s[86:87]
	s_cmp_gt_i32 s1, 15
	s_cselect_b32 s37, s72, s37
	s_bcnt1_i32_b64 s1, s[98:99]
	s_cmp_gt_i32 s1, 15
	s_cselect_b32 s75, s76, s75
	s_bcnt1_i32_b64 s1, s[100:101]
	s_cmp_gt_i32 s1, 15
	s_cselect_b32 s79, s80, s79
	s_or_b32 s52, s32, 0x20000000
	v_cmp_le_u64_e64 s[84:85], s[52:53], v[212:213]
	s_or_b32 s72, s37, 0x20000000
	v_cmp_le_u64_e64 s[86:87], s[72:73], v[214:215]
	s_or_b32 s76, s75, 0x20000000
	v_cmp_le_u64_e64 s[98:99], s[76:77], v[216:217]
	s_or_b32 s80, s79, 0x20000000
	v_cmp_le_u64_e64 s[100:101], s[80:81], v[218:219]
	s_bcnt1_i32_b64 s1, s[84:85]
	s_cmp_gt_i32 s1, 15
	s_cselect_b32 s32, s52, s32
	s_bcnt1_i32_b64 s1, s[86:87]
	s_cmp_gt_i32 s1, 15
	s_cselect_b32 s37, s72, s37
	s_bcnt1_i32_b64 s1, s[98:99]
	s_cmp_gt_i32 s1, 15
	s_cselect_b32 s75, s76, s75
	s_bcnt1_i32_b64 s1, s[100:101]
	s_cmp_gt_i32 s1, 15
	s_cselect_b32 s79, s80, s79
	s_or_b32 s52, s32, 0x10000000
	v_cmp_le_u64_e64 s[84:85], s[52:53], v[212:213]
	s_or_b32 s72, s37, 0x10000000
	v_cmp_le_u64_e64 s[86:87], s[72:73], v[214:215]
	s_or_b32 s76, s75, 0x10000000
	v_cmp_le_u64_e64 s[98:99], s[76:77], v[216:217]
	s_or_b32 s80, s79, 0x10000000
	v_cmp_le_u64_e64 s[100:101], s[80:81], v[218:219]
	s_bcnt1_i32_b64 s1, s[84:85]
	s_cmp_gt_i32 s1, 15
	s_cselect_b32 s32, s52, s32
	s_bcnt1_i32_b64 s1, s[86:87]
	s_cmp_gt_i32 s1, 15
	s_cselect_b32 s37, s72, s37
	s_bcnt1_i32_b64 s1, s[98:99]
	s_cmp_gt_i32 s1, 15
	s_cselect_b32 s75, s76, s75
	s_bcnt1_i32_b64 s1, s[100:101]
	s_cmp_gt_i32 s1, 15
	s_cselect_b32 s79, s80, s79
	s_or_b32 s52, s32, 0x8000000
	v_cmp_le_u64_e64 s[84:85], s[52:53], v[212:213]
	s_or_b32 s72, s37, 0x8000000
	v_cmp_le_u64_e64 s[86:87], s[72:73], v[214:215]
	s_or_b32 s76, s75, 0x8000000
	v_cmp_le_u64_e64 s[98:99], s[76:77], v[216:217]
	s_or_b32 s80, s79, 0x8000000
	v_cmp_le_u64_e64 s[100:101], s[80:81], v[218:219]
	s_bcnt1_i32_b64 s1, s[84:85]
	s_cmp_gt_i32 s1, 15
	s_cselect_b32 s32, s52, s32
	s_bcnt1_i32_b64 s1, s[86:87]
	s_cmp_gt_i32 s1, 15
	s_cselect_b32 s37, s72, s37
	s_bcnt1_i32_b64 s1, s[98:99]
	s_cmp_gt_i32 s1, 15
	s_cselect_b32 s75, s76, s75
	s_bcnt1_i32_b64 s1, s[100:101]
	s_cmp_gt_i32 s1, 15
	s_cselect_b32 s79, s80, s79
	s_or_b32 s52, s32, 0x4000000
	v_cmp_le_u64_e64 s[84:85], s[52:53], v[212:213]
	s_or_b32 s72, s37, 0x4000000
	v_cmp_le_u64_e64 s[86:87], s[72:73], v[214:215]
	s_or_b32 s76, s75, 0x4000000
	v_cmp_le_u64_e64 s[98:99], s[76:77], v[216:217]
	s_or_b32 s80, s79, 0x4000000
	v_cmp_le_u64_e64 s[100:101], s[80:81], v[218:219]
	s_bcnt1_i32_b64 s1, s[84:85]
	s_cmp_gt_i32 s1, 15
	s_cselect_b32 s32, s52, s32
	s_bcnt1_i32_b64 s1, s[86:87]
	s_cmp_gt_i32 s1, 15
	s_cselect_b32 s37, s72, s37
	s_bcnt1_i32_b64 s1, s[98:99]
	s_cmp_gt_i32 s1, 15
	s_cselect_b32 s75, s76, s75
	s_bcnt1_i32_b64 s1, s[100:101]
	s_cmp_gt_i32 s1, 15
	s_cselect_b32 s79, s80, s79
	s_or_b32 s52, s32, 0x2000000
	v_cmp_le_u64_e64 s[84:85], s[52:53], v[212:213]
	s_or_b32 s72, s37, 0x2000000
	v_cmp_le_u64_e64 s[86:87], s[72:73], v[214:215]
	s_or_b32 s76, s75, 0x2000000
	v_cmp_le_u64_e64 s[98:99], s[76:77], v[216:217]
	s_or_b32 s80, s79, 0x2000000
	v_cmp_le_u64_e64 s[100:101], s[80:81], v[218:219]
	s_bcnt1_i32_b64 s1, s[84:85]
	s_cmp_gt_i32 s1, 15
	s_cselect_b32 s32, s52, s32
	s_bcnt1_i32_b64 s1, s[86:87]
	s_cmp_gt_i32 s1, 15
	s_cselect_b32 s37, s72, s37
	s_bcnt1_i32_b64 s1, s[98:99]
	s_cmp_gt_i32 s1, 15
	s_cselect_b32 s75, s76, s75
	s_bcnt1_i32_b64 s1, s[100:101]
	s_cmp_gt_i32 s1, 15
	s_cselect_b32 s79, s80, s79
	s_or_b32 s52, s32, 0x1000000
	v_cmp_le_u64_e64 s[84:85], s[52:53], v[212:213]
	s_or_b32 s72, s37, 0x1000000
	v_cmp_le_u64_e64 s[86:87], s[72:73], v[214:215]
	s_or_b32 s76, s75, 0x1000000
	v_cmp_le_u64_e64 s[98:99], s[76:77], v[216:217]
	s_or_b32 s80, s79, 0x1000000
	v_cmp_le_u64_e64 s[100:101], s[80:81], v[218:219]
	s_bcnt1_i32_b64 s1, s[84:85]
	s_cmp_gt_i32 s1, 15
	s_cselect_b32 s32, s52, s32
	s_bcnt1_i32_b64 s1, s[86:87]
	s_cmp_gt_i32 s1, 15
	s_cselect_b32 s37, s72, s37
	s_bcnt1_i32_b64 s1, s[98:99]
	s_cmp_gt_i32 s1, 15
	s_cselect_b32 s75, s76, s75
	s_bcnt1_i32_b64 s1, s[100:101]
	s_cmp_gt_i32 s1, 15
	s_cselect_b32 s79, s80, s79
	s_or_b32 s52, s32, 0x800000
	v_cmp_le_u64_e64 s[84:85], s[52:53], v[212:213]
	s_or_b32 s72, s37, 0x800000
	v_cmp_le_u64_e64 s[86:87], s[72:73], v[214:215]
	s_or_b32 s76, s75, 0x800000
	v_cmp_le_u64_e64 s[98:99], s[76:77], v[216:217]
	s_or_b32 s80, s79, 0x800000
	v_cmp_le_u64_e64 s[100:101], s[80:81], v[218:219]
	s_bcnt1_i32_b64 s1, s[84:85]
	s_cmp_gt_i32 s1, 15
	s_cselect_b32 s32, s52, s32
	s_bcnt1_i32_b64 s1, s[86:87]
	s_cmp_gt_i32 s1, 15
	s_cselect_b32 s37, s72, s37
	s_bcnt1_i32_b64 s1, s[98:99]
	s_cmp_gt_i32 s1, 15
	s_cselect_b32 s75, s76, s75
	s_bcnt1_i32_b64 s1, s[100:101]
	s_cmp_gt_i32 s1, 15
	s_cselect_b32 s79, s80, s79
	s_or_b32 s52, s32, 0x400000
	v_cmp_le_u64_e64 s[84:85], s[52:53], v[212:213]
	s_or_b32 s72, s37, 0x400000
	v_cmp_le_u64_e64 s[86:87], s[72:73], v[214:215]
	s_or_b32 s76, s75, 0x400000
	v_cmp_le_u64_e64 s[98:99], s[76:77], v[216:217]
	s_or_b32 s80, s79, 0x400000
	v_cmp_le_u64_e64 s[100:101], s[80:81], v[218:219]
	s_bcnt1_i32_b64 s1, s[84:85]
	s_cmp_gt_i32 s1, 15
	s_cselect_b32 s32, s52, s32
	s_bcnt1_i32_b64 s1, s[86:87]
	s_cmp_gt_i32 s1, 15
	s_cselect_b32 s37, s72, s37
	s_bcnt1_i32_b64 s1, s[98:99]
	s_cmp_gt_i32 s1, 15
	s_cselect_b32 s75, s76, s75
	s_bcnt1_i32_b64 s1, s[100:101]
	s_cmp_gt_i32 s1, 15
	s_cselect_b32 s79, s80, s79
	s_or_b32 s52, s32, 0x200000
	v_cmp_le_u64_e64 s[84:85], s[52:53], v[212:213]
	s_or_b32 s72, s37, 0x200000
	v_cmp_le_u64_e64 s[86:87], s[72:73], v[214:215]
	s_or_b32 s76, s75, 0x200000
	v_cmp_le_u64_e64 s[98:99], s[76:77], v[216:217]
	s_or_b32 s80, s79, 0x200000
	v_cmp_le_u64_e64 s[100:101], s[80:81], v[218:219]
	s_bcnt1_i32_b64 s1, s[84:85]
	s_cmp_gt_i32 s1, 15
	s_cselect_b32 s32, s52, s32
	s_bcnt1_i32_b64 s1, s[86:87]
	s_cmp_gt_i32 s1, 15
	s_cselect_b32 s37, s72, s37
	s_bcnt1_i32_b64 s1, s[98:99]
	s_cmp_gt_i32 s1, 15
	s_cselect_b32 s75, s76, s75
	s_bcnt1_i32_b64 s1, s[100:101]
	s_cmp_gt_i32 s1, 15
	s_cselect_b32 s79, s80, s79
	s_or_b32 s52, s32, 0x100000
	v_cmp_le_u64_e64 s[84:85], s[52:53], v[212:213]
	s_or_b32 s72, s37, 0x100000
	v_cmp_le_u64_e64 s[86:87], s[72:73], v[214:215]
	s_or_b32 s76, s75, 0x100000
	v_cmp_le_u64_e64 s[98:99], s[76:77], v[216:217]
	s_or_b32 s80, s79, 0x100000
	v_cmp_le_u64_e64 s[100:101], s[80:81], v[218:219]
	s_bcnt1_i32_b64 s1, s[84:85]
	s_cmp_gt_i32 s1, 15
	s_cselect_b32 s32, s52, s32
	s_bcnt1_i32_b64 s1, s[86:87]
	s_cmp_gt_i32 s1, 15
	s_cselect_b32 s37, s72, s37
	s_bcnt1_i32_b64 s1, s[98:99]
	s_cmp_gt_i32 s1, 15
	s_cselect_b32 s75, s76, s75
	s_bcnt1_i32_b64 s1, s[100:101]
	s_cmp_gt_i32 s1, 15
	s_cselect_b32 s79, s80, s79
	s_or_b32 s52, s32, 0x80000
	v_cmp_le_u64_e64 s[84:85], s[52:53], v[212:213]
	s_or_b32 s72, s37, 0x80000
	v_cmp_le_u64_e64 s[86:87], s[72:73], v[214:215]
	s_or_b32 s76, s75, 0x80000
	v_cmp_le_u64_e64 s[98:99], s[76:77], v[216:217]
	s_or_b32 s80, s79, 0x80000
	v_cmp_le_u64_e64 s[100:101], s[80:81], v[218:219]
	s_bcnt1_i32_b64 s1, s[84:85]
	s_cmp_gt_i32 s1, 15
	s_cselect_b32 s32, s52, s32
	s_bcnt1_i32_b64 s1, s[86:87]
	s_cmp_gt_i32 s1, 15
	s_cselect_b32 s37, s72, s37
	s_bcnt1_i32_b64 s1, s[98:99]
	s_cmp_gt_i32 s1, 15
	s_cselect_b32 s75, s76, s75
	s_bcnt1_i32_b64 s1, s[100:101]
	s_cmp_gt_i32 s1, 15
	s_cselect_b32 s79, s80, s79
	s_or_b32 s52, s32, 0x40000
	v_cmp_le_u64_e64 s[84:85], s[52:53], v[212:213]
	s_or_b32 s72, s37, 0x40000
	v_cmp_le_u64_e64 s[86:87], s[72:73], v[214:215]
	s_or_b32 s76, s75, 0x40000
	v_cmp_le_u64_e64 s[98:99], s[76:77], v[216:217]
	s_or_b32 s80, s79, 0x40000
	v_cmp_le_u64_e64 s[100:101], s[80:81], v[218:219]
	s_bcnt1_i32_b64 s1, s[84:85]
	s_cmp_gt_i32 s1, 15
	s_cselect_b32 s32, s52, s32
	s_bcnt1_i32_b64 s1, s[86:87]
	s_cmp_gt_i32 s1, 15
	s_cselect_b32 s37, s72, s37
	s_bcnt1_i32_b64 s1, s[98:99]
	s_cmp_gt_i32 s1, 15
	s_cselect_b32 s75, s76, s75
	s_bcnt1_i32_b64 s1, s[100:101]
	s_cmp_gt_i32 s1, 15
	s_cselect_b32 s79, s80, s79
	s_or_b32 s52, s32, 0x20000
	v_cmp_le_u64_e64 s[84:85], s[52:53], v[212:213]
	s_or_b32 s72, s37, 0x20000
	v_cmp_le_u64_e64 s[86:87], s[72:73], v[214:215]
	s_or_b32 s76, s75, 0x20000
	v_cmp_le_u64_e64 s[98:99], s[76:77], v[216:217]
	s_or_b32 s80, s79, 0x20000
	v_cmp_le_u64_e64 s[100:101], s[80:81], v[218:219]
	s_bcnt1_i32_b64 s1, s[84:85]
	s_cmp_gt_i32 s1, 15
	s_cselect_b32 s32, s52, s32
	s_bcnt1_i32_b64 s1, s[86:87]
	s_cmp_gt_i32 s1, 15
	s_cselect_b32 s37, s72, s37
	s_bcnt1_i32_b64 s1, s[98:99]
	s_cmp_gt_i32 s1, 15
	s_cselect_b32 s75, s76, s75
	s_bcnt1_i32_b64 s1, s[100:101]
	s_cmp_gt_i32 s1, 15
	s_cselect_b32 s79, s80, s79
	s_or_b32 s52, s32, 0x10000
	v_cmp_le_u64_e64 s[84:85], s[52:53], v[212:213]
	s_or_b32 s72, s37, 0x10000
	v_cmp_le_u64_e64 s[86:87], s[72:73], v[214:215]
	s_or_b32 s76, s75, 0x10000
	v_cmp_le_u64_e64 s[98:99], s[76:77], v[216:217]
	s_or_b32 s80, s79, 0x10000
	v_cmp_le_u64_e64 s[100:101], s[80:81], v[218:219]
	s_bcnt1_i32_b64 s1, s[84:85]
	s_cmp_gt_i32 s1, 15
	s_cselect_b32 s32, s52, s32
	s_bcnt1_i32_b64 s1, s[86:87]
	s_cmp_gt_i32 s1, 15
	s_cselect_b32 s37, s72, s37
	s_bcnt1_i32_b64 s1, s[98:99]
	s_cmp_gt_i32 s1, 15
	s_cselect_b32 s75, s76, s75
	s_bcnt1_i32_b64 s1, s[100:101]
	s_cmp_gt_i32 s1, 15
	s_cselect_b32 s79, s80, s79
	s_or_b32 s52, s32, 0x8000
	v_cmp_le_u64_e64 s[84:85], s[52:53], v[212:213]
	s_or_b32 s72, s37, 0x8000
	v_cmp_le_u64_e64 s[86:87], s[72:73], v[214:215]
	s_or_b32 s76, s75, 0x8000
	v_cmp_le_u64_e64 s[98:99], s[76:77], v[216:217]
	s_or_b32 s80, s79, 0x8000
	v_cmp_le_u64_e64 s[100:101], s[80:81], v[218:219]
	s_bcnt1_i32_b64 s1, s[84:85]
	s_cmp_gt_i32 s1, 15
	s_cselect_b32 s32, s52, s32
	s_bcnt1_i32_b64 s1, s[86:87]
	s_cmp_gt_i32 s1, 15
	s_cselect_b32 s37, s72, s37
	s_bcnt1_i32_b64 s1, s[98:99]
	s_cmp_gt_i32 s1, 15
	s_cselect_b32 s75, s76, s75
	s_bcnt1_i32_b64 s1, s[100:101]
	s_cmp_gt_i32 s1, 15
	s_cselect_b32 s79, s80, s79
	s_or_b32 s52, s32, 0x4000
	v_cmp_le_u64_e64 s[84:85], s[52:53], v[212:213]
	s_or_b32 s72, s37, 0x4000
	v_cmp_le_u64_e64 s[86:87], s[72:73], v[214:215]
	s_or_b32 s76, s75, 0x4000
	v_cmp_le_u64_e64 s[98:99], s[76:77], v[216:217]
	s_or_b32 s80, s79, 0x4000
	v_cmp_le_u64_e64 s[100:101], s[80:81], v[218:219]
	s_bcnt1_i32_b64 s1, s[84:85]
	s_cmp_gt_i32 s1, 15
	s_cselect_b32 s32, s52, s32
	s_bcnt1_i32_b64 s1, s[86:87]
	s_cmp_gt_i32 s1, 15
	s_cselect_b32 s37, s72, s37
	s_bcnt1_i32_b64 s1, s[98:99]
	s_cmp_gt_i32 s1, 15
	s_cselect_b32 s75, s76, s75
	s_bcnt1_i32_b64 s1, s[100:101]
	s_cmp_gt_i32 s1, 15
	s_cselect_b32 s79, s80, s79
	s_or_b32 s52, s32, 0x2000
	v_cmp_le_u64_e64 s[84:85], s[52:53], v[212:213]
	s_or_b32 s72, s37, 0x2000
	v_cmp_le_u64_e64 s[86:87], s[72:73], v[214:215]
	s_or_b32 s76, s75, 0x2000
	v_cmp_le_u64_e64 s[98:99], s[76:77], v[216:217]
	s_or_b32 s80, s79, 0x2000
	v_cmp_le_u64_e64 s[100:101], s[80:81], v[218:219]
	s_bcnt1_i32_b64 s1, s[84:85]
	s_cmp_gt_i32 s1, 15
	s_cselect_b32 s32, s52, s32
	s_bcnt1_i32_b64 s1, s[86:87]
	s_cmp_gt_i32 s1, 15
	s_cselect_b32 s37, s72, s37
	s_bcnt1_i32_b64 s1, s[98:99]
	s_cmp_gt_i32 s1, 15
	s_cselect_b32 s75, s76, s75
	s_bcnt1_i32_b64 s1, s[100:101]
	s_cmp_gt_i32 s1, 15
	s_cselect_b32 s79, s80, s79
	s_or_b32 s52, s32, 0x1000
	v_cmp_le_u64_e64 s[84:85], s[52:53], v[212:213]
	s_or_b32 s72, s37, 0x1000
	v_cmp_le_u64_e64 s[86:87], s[72:73], v[214:215]
	s_or_b32 s76, s75, 0x1000
	v_cmp_le_u64_e64 s[98:99], s[76:77], v[216:217]
	s_or_b32 s80, s79, 0x1000
	v_cmp_le_u64_e64 s[100:101], s[80:81], v[218:219]
	s_bcnt1_i32_b64 s1, s[84:85]
	s_cmp_gt_i32 s1, 15
	s_cselect_b32 s32, s52, s32
	s_bcnt1_i32_b64 s1, s[86:87]
	s_cmp_gt_i32 s1, 15
	s_cselect_b32 s37, s72, s37
	s_bcnt1_i32_b64 s1, s[98:99]
	s_cmp_gt_i32 s1, 15
	s_cselect_b32 s75, s76, s75
	s_bcnt1_i32_b64 s1, s[100:101]
	s_cmp_gt_i32 s1, 15
	s_cselect_b32 s79, s80, s79
	s_or_b32 s52, s32, 0x800
	v_cmp_le_u64_e64 s[84:85], s[52:53], v[212:213]
	s_or_b32 s72, s37, 0x800
	v_cmp_le_u64_e64 s[86:87], s[72:73], v[214:215]
	s_or_b32 s76, s75, 0x800
	v_cmp_le_u64_e64 s[98:99], s[76:77], v[216:217]
	s_or_b32 s80, s79, 0x800
	v_cmp_le_u64_e64 s[100:101], s[80:81], v[218:219]
	s_bcnt1_i32_b64 s1, s[84:85]
	s_cmp_gt_i32 s1, 15
	s_cselect_b32 s32, s52, s32
	s_bcnt1_i32_b64 s1, s[86:87]
	s_cmp_gt_i32 s1, 15
	s_cselect_b32 s37, s72, s37
	s_bcnt1_i32_b64 s1, s[98:99]
	s_cmp_gt_i32 s1, 15
	s_cselect_b32 s75, s76, s75
	s_bcnt1_i32_b64 s1, s[100:101]
	s_cmp_gt_i32 s1, 15
	s_cselect_b32 s79, s80, s79
	s_or_b32 s52, s32, 0x400
	v_cmp_le_u64_e64 s[84:85], s[52:53], v[212:213]
	s_or_b32 s72, s37, 0x400
	v_cmp_le_u64_e64 s[86:87], s[72:73], v[214:215]
	s_or_b32 s76, s75, 0x400
	v_cmp_le_u64_e64 s[98:99], s[76:77], v[216:217]
	s_or_b32 s80, s79, 0x400
	v_cmp_le_u64_e64 s[100:101], s[80:81], v[218:219]
	s_bcnt1_i32_b64 s1, s[84:85]
	s_cmp_gt_i32 s1, 15
	s_cselect_b32 s32, s52, s32
	s_bcnt1_i32_b64 s1, s[86:87]
	s_cmp_gt_i32 s1, 15
	s_cselect_b32 s37, s72, s37
	s_bcnt1_i32_b64 s1, s[98:99]
	s_cmp_gt_i32 s1, 15
	s_cselect_b32 s75, s76, s75
	s_bcnt1_i32_b64 s1, s[100:101]
	s_cmp_gt_i32 s1, 15
	s_cselect_b32 s79, s80, s79
	s_or_b32 s52, s32, 0x200
	v_cmp_le_u64_e64 s[84:85], s[52:53], v[212:213]
	s_or_b32 s72, s37, 0x200
	v_cmp_le_u64_e64 s[86:87], s[72:73], v[214:215]
	s_or_b32 s76, s75, 0x200
	v_cmp_le_u64_e64 s[98:99], s[76:77], v[216:217]
	s_or_b32 s80, s79, 0x200
	v_cmp_le_u64_e64 s[100:101], s[80:81], v[218:219]
	s_bcnt1_i32_b64 s1, s[84:85]
	s_cmp_gt_i32 s1, 15
	s_cselect_b32 s32, s52, s32
	s_bcnt1_i32_b64 s1, s[86:87]
	s_cmp_gt_i32 s1, 15
	s_cselect_b32 s37, s72, s37
	s_bcnt1_i32_b64 s1, s[98:99]
	s_cmp_gt_i32 s1, 15
	s_cselect_b32 s75, s76, s75
	s_bcnt1_i32_b64 s1, s[100:101]
	s_cmp_gt_i32 s1, 15
	s_cselect_b32 s79, s80, s79
	s_or_b32 s52, s32, 0x100
	v_cmp_le_u64_e64 s[84:85], s[52:53], v[212:213]
	s_or_b32 s72, s37, 0x100
	v_cmp_le_u64_e64 s[86:87], s[72:73], v[214:215]
	s_or_b32 s76, s75, 0x100
	v_cmp_le_u64_e64 s[98:99], s[76:77], v[216:217]
	s_or_b32 s80, s79, 0x100
	v_cmp_le_u64_e64 s[100:101], s[80:81], v[218:219]
	s_bcnt1_i32_b64 s1, s[84:85]
	s_cmp_gt_i32 s1, 15
	s_cselect_b32 s32, s52, s32
	s_bcnt1_i32_b64 s1, s[86:87]
	s_cmp_gt_i32 s1, 15
	s_cselect_b32 s37, s72, s37
	s_bcnt1_i32_b64 s1, s[98:99]
	s_cmp_gt_i32 s1, 15
	s_cselect_b32 s75, s76, s75
	s_bcnt1_i32_b64 s1, s[100:101]
	s_cmp_gt_i32 s1, 15
	s_cselect_b32 s79, s80, s79
	s_or_b32 s52, s32, 0x80
	v_cmp_le_u64_e64 s[84:85], s[52:53], v[212:213]
	s_or_b32 s72, s37, 0x80
	v_cmp_le_u64_e64 s[86:87], s[72:73], v[214:215]
	s_or_b32 s76, s75, 0x80
	v_cmp_le_u64_e64 s[98:99], s[76:77], v[216:217]
	s_or_b32 s80, s79, 0x80
	v_cmp_le_u64_e64 s[100:101], s[80:81], v[218:219]
	s_bcnt1_i32_b64 s1, s[84:85]
	s_cmp_gt_i32 s1, 15
	s_cselect_b32 s32, s52, s32
	s_bcnt1_i32_b64 s1, s[86:87]
	s_cmp_gt_i32 s1, 15
	s_cselect_b32 s37, s72, s37
	s_bcnt1_i32_b64 s1, s[98:99]
	s_cmp_gt_i32 s1, 15
	s_cselect_b32 s75, s76, s75
	s_bcnt1_i32_b64 s1, s[100:101]
	s_cmp_gt_i32 s1, 15
	s_cselect_b32 s79, s80, s79
	s_or_b32 s52, s32, 0x40
	v_cmp_le_u64_e64 s[84:85], s[52:53], v[212:213]
	s_or_b32 s72, s37, 0x40
	v_cmp_le_u64_e64 s[86:87], s[72:73], v[214:215]
	s_or_b32 s76, s75, 0x40
	v_cmp_le_u64_e64 s[98:99], s[76:77], v[216:217]
	s_or_b32 s80, s79, 0x40
	v_cmp_le_u64_e64 s[100:101], s[80:81], v[218:219]
	s_bcnt1_i32_b64 s1, s[84:85]
	s_cmp_gt_i32 s1, 15
	s_cselect_b32 s32, s52, s32
	s_bcnt1_i32_b64 s1, s[86:87]
	s_cmp_gt_i32 s1, 15
	s_cselect_b32 s37, s72, s37
	s_bcnt1_i32_b64 s1, s[98:99]
	s_cmp_gt_i32 s1, 15
	s_cselect_b32 s75, s76, s75
	s_bcnt1_i32_b64 s1, s[100:101]
	s_cmp_gt_i32 s1, 15
	s_cselect_b32 s79, s80, s79
	s_or_b32 s52, s32, 0x20
	v_cmp_le_u64_e64 s[84:85], s[52:53], v[212:213]
	s_or_b32 s72, s37, 0x20
	v_cmp_le_u64_e64 s[86:87], s[72:73], v[214:215]
	s_or_b32 s76, s75, 0x20
	v_cmp_le_u64_e64 s[98:99], s[76:77], v[216:217]
	s_or_b32 s80, s79, 0x20
	v_cmp_le_u64_e64 s[100:101], s[80:81], v[218:219]
	s_bcnt1_i32_b64 s1, s[84:85]
	s_cmp_gt_i32 s1, 15
	s_cselect_b32 s32, s52, s32
	s_bcnt1_i32_b64 s1, s[86:87]
	s_cmp_gt_i32 s1, 15
	s_cselect_b32 s37, s72, s37
	s_bcnt1_i32_b64 s1, s[98:99]
	s_cmp_gt_i32 s1, 15
	s_cselect_b32 s75, s76, s75
	s_bcnt1_i32_b64 s1, s[100:101]
	s_cmp_gt_i32 s1, 15
	s_cselect_b32 s79, s80, s79
	s_or_b32 s52, s32, 0x10
	v_cmp_le_u64_e64 s[84:85], s[52:53], v[212:213]
	s_or_b32 s72, s37, 0x10
	v_cmp_le_u64_e64 s[86:87], s[72:73], v[214:215]
	s_or_b32 s76, s75, 0x10
	v_cmp_le_u64_e64 s[98:99], s[76:77], v[216:217]
	s_or_b32 s80, s79, 0x10
	v_cmp_le_u64_e64 s[100:101], s[80:81], v[218:219]
	s_bcnt1_i32_b64 s1, s[84:85]
	s_cmp_gt_i32 s1, 15
	s_cselect_b32 s32, s52, s32
	s_bcnt1_i32_b64 s1, s[86:87]
	s_cmp_gt_i32 s1, 15
	s_cselect_b32 s37, s72, s37
	s_bcnt1_i32_b64 s1, s[98:99]
	s_cmp_gt_i32 s1, 15
	s_cselect_b32 s75, s76, s75
	s_bcnt1_i32_b64 s1, s[100:101]
	s_cmp_gt_i32 s1, 15
	s_cselect_b32 s79, s80, s79
	s_or_b32 s52, s32, 0x8
	v_cmp_le_u64_e64 s[84:85], s[52:53], v[212:213]
	s_or_b32 s72, s37, 0x8
	v_cmp_le_u64_e64 s[86:87], s[72:73], v[214:215]
	s_or_b32 s76, s75, 0x8
	v_cmp_le_u64_e64 s[98:99], s[76:77], v[216:217]
	s_or_b32 s80, s79, 0x8
	v_cmp_le_u64_e64 s[100:101], s[80:81], v[218:219]
	s_bcnt1_i32_b64 s1, s[84:85]
	s_cmp_gt_i32 s1, 15
	s_cselect_b32 s32, s52, s32
	s_bcnt1_i32_b64 s1, s[86:87]
	s_cmp_gt_i32 s1, 15
	s_cselect_b32 s37, s72, s37
	s_bcnt1_i32_b64 s1, s[98:99]
	s_cmp_gt_i32 s1, 15
	s_cselect_b32 s75, s76, s75
	s_bcnt1_i32_b64 s1, s[100:101]
	s_cmp_gt_i32 s1, 15
	s_cselect_b32 s79, s80, s79
	s_or_b32 s52, s32, 0x4
	v_cmp_le_u64_e64 s[84:85], s[52:53], v[212:213]
	s_or_b32 s72, s37, 0x4
	v_cmp_le_u64_e64 s[86:87], s[72:73], v[214:215]
	s_or_b32 s76, s75, 0x4
	v_cmp_le_u64_e64 s[98:99], s[76:77], v[216:217]
	s_or_b32 s80, s79, 0x4
	v_cmp_le_u64_e64 s[100:101], s[80:81], v[218:219]
	s_bcnt1_i32_b64 s1, s[84:85]
	s_cmp_gt_i32 s1, 15
	s_cselect_b32 s32, s52, s32
	s_bcnt1_i32_b64 s1, s[86:87]
	s_cmp_gt_i32 s1, 15
	s_cselect_b32 s37, s72, s37
	s_bcnt1_i32_b64 s1, s[98:99]
	s_cmp_gt_i32 s1, 15
	s_cselect_b32 s75, s76, s75
	s_bcnt1_i32_b64 s1, s[100:101]
	s_cmp_gt_i32 s1, 15
	s_cselect_b32 s79, s80, s79
	s_or_b32 s52, s32, 0x2
	v_cmp_le_u64_e64 s[84:85], s[52:53], v[212:213]
	s_or_b32 s72, s37, 0x2
	v_cmp_le_u64_e64 s[86:87], s[72:73], v[214:215]
	s_or_b32 s76, s75, 0x2
	v_cmp_le_u64_e64 s[98:99], s[76:77], v[216:217]
	s_or_b32 s80, s79, 0x2
	v_cmp_le_u64_e64 s[100:101], s[80:81], v[218:219]
	s_bcnt1_i32_b64 s1, s[84:85]
	s_cmp_gt_i32 s1, 15
	s_cselect_b32 s32, s52, s32
	s_bcnt1_i32_b64 s1, s[86:87]
	s_cmp_gt_i32 s1, 15
	s_cselect_b32 s37, s72, s37
	s_bcnt1_i32_b64 s1, s[98:99]
	s_cmp_gt_i32 s1, 15
	s_cselect_b32 s75, s76, s75
	s_bcnt1_i32_b64 s1, s[100:101]
	s_cmp_gt_i32 s1, 15
	s_cselect_b32 s79, s80, s79
	s_or_b32 s52, s32, 0x1
	v_cmp_le_u64_e64 s[84:85], s[52:53], v[212:213]
	s_or_b32 s72, s37, 0x1
	v_cmp_le_u64_e64 s[86:87], s[72:73], v[214:215]
	s_or_b32 s76, s75, 0x1
	v_cmp_le_u64_e64 s[98:99], s[76:77], v[216:217]
	s_or_b32 s80, s79, 0x1
	v_cmp_le_u64_e64 s[100:101], s[80:81], v[218:219]
	s_bcnt1_i32_b64 s1, s[84:85]
	s_cmp_gt_i32 s1, 15
	s_cselect_b32 s32, s52, s32
	s_bcnt1_i32_b64 s1, s[86:87]
	s_cmp_gt_i32 s1, 15
	s_cselect_b32 s37, s72, s37
	s_bcnt1_i32_b64 s1, s[98:99]
	s_cmp_gt_i32 s1, 15
	s_cselect_b32 s75, s76, s75
	s_bcnt1_i32_b64 s1, s[100:101]
	s_cmp_gt_i32 s1, 15
	s_cselect_b32 s79, s80, s79
	s_mov_b32 s52, s32
	s_mov_b32 s72, s37
	s_mov_b32 s76, s75
	s_mov_b32 s80, s79
	s_mov_b32 s1, 0xf0c9f2ca
	v_cmp_le_u64_e64 s[18:19], s[52:53], v[212:213]
	v_cmp_lt_f32_e64 s[20:21], s1, v220
	s_and_b64 s[4:5], s[18:19], s[20:21]
	v_cndmask_b32_e64 v0, 0, 1, s[4:5]
	v_cmp_ne_u32_e64 s[18:19], 0, v0
	s_and_saveexec_b64 s[4:5], s[46:47]
	s_cbranch_execz .Ltk_w0
	s_add_i32 s1, s6, 0
	v_mov_b32_e32 v0, s1
	v_mov_b64_e32 v[6:7], s[18:19]
	s_waitcnt vmcnt(0)
	ds_write_b64 v0, v[6:7]
.Ltk_w0:
	s_or_b64 exec, exec, s[4:5]
	s_mov_b32 s1, 0xf0c9f2ca
	v_cmp_le_u64_e64 s[18:19], s[72:73], v[214:215]
	v_cmp_lt_f32_e64 s[20:21], s1, v221
	s_and_b64 s[4:5], s[18:19], s[20:21]
	v_cndmask_b32_e64 v0, 0, 1, s[4:5]
	v_cmp_ne_u32_e64 s[18:19], 0, v0
	s_and_saveexec_b64 s[4:5], s[46:47]
	s_cbranch_execz .Ltk_w1
	s_add_i32 s1, s6, 8
	v_mov_b32_e32 v0, s1
	v_mov_b64_e32 v[6:7], s[18:19]
	s_waitcnt vmcnt(0)
	ds_write_b64 v0, v[6:7]
.Ltk_w1:
	s_or_b64 exec, exec, s[4:5]
	s_mov_b32 s1, 0xf0c9f2ca
	v_cmp_le_u64_e64 s[18:19], s[76:77], v[216:217]
	v_cmp_lt_f32_e64 s[20:21], s1, v222
	s_and_b64 s[4:5], s[18:19], s[20:21]
	v_cndmask_b32_e64 v0, 0, 1, s[4:5]
	v_cmp_ne_u32_e64 s[18:19], 0, v0
	s_and_saveexec_b64 s[4:5], s[46:47]
	s_cbranch_execz .Ltk_w2
	s_add_i32 s1, s6, 16
	v_mov_b32_e32 v0, s1
	v_mov_b64_e32 v[6:7], s[18:19]
	s_waitcnt vmcnt(0)
	ds_write_b64 v0, v[6:7]
.Ltk_w2:
	s_or_b64 exec, exec, s[4:5]
	s_mov_b32 s1, 0xf0c9f2ca
	v_cmp_le_u64_e64 s[18:19], s[80:81], v[218:219]
	v_cmp_lt_f32_e64 s[20:21], s1, v223
	s_and_b64 s[4:5], s[18:19], s[20:21]
	v_cndmask_b32_e64 v0, 0, 1, s[4:5]
	v_cmp_ne_u32_e64 s[18:19], 0, v0
	s_and_saveexec_b64 s[4:5], s[46:47]
	s_cbranch_execz .Ltk_w3
	s_add_i32 s1, s6, 24
	v_mov_b32_e32 v0, s1
	v_mov_b64_e32 v[6:7], s[18:19]
	s_waitcnt vmcnt(0)
	ds_write_b64 v0, v[6:7]
.Ltk_w3:
	s_or_b64 exec, exec, s[4:5]
	s_branch .LBB0_1692

	.amdhsa_kernel _Z8mega_fwd4Args
		.amdhsa_group_segment_fixed_size 0
		.amdhsa_private_segment_fixed_size 0
		.amdhsa_kernarg_size 520
		.amdhsa_user_sgpr_count 2
		.amdhsa_user_sgpr_dispatch_ptr 0
		.amdhsa_user_sgpr_queue_ptr 0
		.amdhsa_user_sgpr_kernarg_segment_ptr 1
		.amdhsa_user_sgpr_dispatch_id 0
		.amdhsa_user_sgpr_kernarg_preload_length 0
		.amdhsa_user_sgpr_kernarg_preload_offset 0
		.amdhsa_user_sgpr_private_segment_size 0
		.amdhsa_uses_dynamic_stack 0
		.amdhsa_enable_private_segment 0
		.amdhsa_system_sgpr_workgroup_id_x 1
		.amdhsa_system_sgpr_workgroup_id_y 0
		.amdhsa_system_sgpr_workgroup_id_z 0
		.amdhsa_system_sgpr_workgroup_info 0
		.amdhsa_system_vgpr_workitem_id 0
		.amdhsa_next_free_vgpr 256
		.amdhsa_next_free_sgpr 102
		.amdhsa_accum_offset 256
		.amdhsa_reserve_vcc 1
		.amdhsa_float_round_mode_32 0
		.amdhsa_float_round_mode_16_64 0
		.amdhsa_float_denorm_mode_32 3
		.amdhsa_float_denorm_mode_16_64 3
		.amdhsa_dx10_clamp 1
		.amdhsa_ieee_mode 1
		.amdhsa_fp16_overflow 0
		.amdhsa_tg_split 0
		.amdhsa_exception_fp_ieee_invalid_op 0
		.amdhsa_exception_fp_denorm_src 0
		.amdhsa_exception_fp_ieee_div_zero 0
		.amdhsa_exception_fp_ieee_overflow 0
		.amdhsa_exception_fp_ieee_underflow 0
		.amdhsa_exception_fp_ieee_inexact 0
		.amdhsa_exception_int_div_zero 0
	.end_amdhsa_kernel

amdhsa.kernels:
  - .agpr_count:     0
    .args:
      - .offset:         0
        .size:           264
        .value_kind:     by_value
      - .offset:         264
        .size:           4
        .value_kind:     hidden_block_count_x
      - .offset:         268
        .size:           4
        .value_kind:     hidden_block_count_y
      - .offset:         272
        .size:           4
        .value_kind:     hidden_block_count_z
      - .offset:         276
        .size:           2
        .value_kind:     hidden_group_size_x
      - .offset:         278
        .size:           2
        .value_kind:     hidden_group_size_y
      - .offset:         280
        .size:           2
        .value_kind:     hidden_group_size_z
      - .offset:         282
        .size:           2
        .value_kind:     hidden_remainder_x
      - .offset:         284
        .size:           2
        .value_kind:     hidden_remainder_y
      - .offset:         286
        .size:           2
        .value_kind:     hidden_remainder_z
      - .offset:         304
        .size:           8
        .value_kind:     hidden_global_offset_x
      - .offset:         312
        .size:           8
        .value_kind:     hidden_global_offset_y
      - .offset:         320
        .size:           8
        .value_kind:     hidden_global_offset_z
      - .offset:         328
        .size:           2
        .value_kind:     hidden_grid_dims
      - .offset:         384
        .size:           4
        .value_kind:     hidden_dynamic_lds_size
    .group_segment_fixed_size: 0
    .kernarg_segment_align: 8
    .kernarg_segment_size: 520
    .language:       OpenCL C
    .language_version:
      - 2
      - 0
    .max_flat_workgroup_size: 512
    .name:           _Z8mega_fwd4Args
    .private_segment_fixed_size: 0
    .sgpr_count:     108
    .sgpr_spill_count: 93
    .symbol:         _Z8mega_fwd4Args.kd
    .uniform_work_group_size: 1
    .uses_dynamic_stack: false
    .vgpr_count:     256
    .vgpr_spill_count: 0
    .wavefront_size: 64
